# 8 conversion units per wave inside the top-k token loop (every 4th token), 12 in the attention loop, 4-5 left in phase 2
# baseline (speedup 1.0000x reference)
; #define LAS __attribute__((address_space(3)))
; __device__ __forceinline__ void convert_experts(Frame& F, int lo, int hi) {
;     const int gw = F.vcu * 8 + F.wave, NGW = F.G * 8;
;     LAS unsigned char* scr = F.lds + F.wave * 16384;
;     unsigned char* W1t = WSP(F, WS_W1T, unsigned char); unsigned char* W2t = WSP(F, WS_W2T, unsigned char);
;     const float* weg = F.a->in[I_WEG]; const float* weu = F.a->in[I_WEU]; const float* wed = F.a->in[I_WED];
;     const float* wsg = F.a->in[I_WSG]; const float* wsu = F.a->in[I_WSU]; const float* wsd = F.a->in[I_WSD];
;     ...
;     constexpr int NPAIRS = CONV_ITEMS / 2;
;     (void)lo; (void)hi;
;     ...
;     if (gw < NPAIRS) {
;         const int ns = 2 * ((NPAIRS - gw + NGW - 1) / NGW);
;         int sq = 0, r = CONV_RIDX(0);
;         TItem tc, tn; CONV_DESC(r, tc); tn = tc;
.Lcv1_vcu:
	s_lshl_b32 s11, s11, 3
	s_add_u32 s89, s11, s9
	s_lshl_b32 s71, s8, 3
	s_mul_i32 s10, s71, 20
	s_add_u32 s89, s89, s10
	s_mov_b32 s69, s89
	s_add_u32 s86, s84, 0x9180000
	s_addc_u32 s87, s85, 0
	s_add_u32 s84, s84, 0x1100000
	s_addc_u32 s85, s85, 0
	s_mov_b32 s90, 0xc2b8aa3b
	s_cmp_ge_u32 s89, 49344
	s_cbranch_scc1 .Lcv1_done
	s_cmp_lt_u32 s69, 49344
	s_cbranch_scc0 .Lcv1_dummyA1
	s_lshr_b32 s10, s69, 6
	s_and_b32 s12, s69, 63
	s_mul_hi_u32 s14, s10, 0xaaaaaaab
	s_lshr_b32 s14, s14, 1
	s_mul_i32 s11, s14, 3
	s_sub_u32 s11, s10, s11
	s_cmp_lt_u32 s14, 256
	s_cselect_b32 s10, s14, 0
	s_cselect_b64 s[44:45], -1, 0
	s_lshl_b32 s10, s10, 20
	s_cmp_eq_u32 s11, 2
	s_cbranch_scc1 .Lcv1_downA1
	s_cmp_eq_u32 s11, 0
	s_cselect_b64 s[4:5], s[72:73], s[74:75]
	s_cselect_b64 s[38:39], s[78:79], s[80:81]
	s_mov_b32 s94, 0xc3317218
	s_cselect_b32 s94, s90, s94
	s_cmp_lg_u64 s[44:45], 0
	s_cselect_b64 s[4:5], s[4:5], s[38:39]
	s_lshr_b32 s38, s12, 3
	s_and_b32 s39, s12, 7
	s_lshl_b32 s8, s38, 17
	s_add_u32 s10, s10, s8
	s_lshl_b32 s8, s39, 7
	s_add_u32 s10, s10, s8
	s_add_u32 s4, s4, s10
	s_addc_u32 s5, s5, 0
	s_lshl_b32 s14, s14, 19
	s_lshr_b32 s8, s39, 2
	s_lshl_b32 s8, s8, 18
	s_add_u32 s14, s14, s8
	s_and_b32 s8, s39, 3
	s_lshl_b32 s8, s8, 15
	s_add_u32 s14, s14, s8
	s_lshl_b32 s8, s11, 17
	s_add_u32 s14, s14, s8
	s_lshl_b32 s8, s38, 7
	s_add_u32 s14, s14, s8
	s_add_u32 s92, s84, s14
	s_addc_u32 s93, s85, 0
	s_movk_i32 s25, 0x400
	s_movk_i32 s27, 0x1000
	s_movk_i32 s8, 0x400
	s_movk_i32 s9, 0x4000
	s_branch .Lcv1_goA1

; #define LAS __attribute__((address_space(3)))
; __device__ __forceinline__ void router_topk(Frame& F, int tile) {
;     const float* logits = WSP(F, WS_B, float); const float* br = F.a->in[I_BR];
;     int* tk_e = WSP(F, WS_TOPK_E, int); float* tk_g = WSP(F, WS_TOPK_G, float); int* tk_p = WSP(F, WS_TOPK_P, int);
;     int* gcnt = (int*)(F.a->ws + WS_CTL + CTL_CNT);
;     LAS int* hist = (LAS int*)F.lds; LAS int* base = hist + 256;
;     const int lane = F.lane, w = F.wave;
;     if (F.tid < 256) hist[F.tid] = 0;
;     __syncthreads();
;     const f32x4 bias = *(const f32x4*)(br + 4 * lane);
;     f32x4 lgn = *(const f32x4*)(logits + (size_t)(tile * 256 + w * 32) * 256 + 4 * lane);
;     int pe = 0, pp = 0; float pg = 0.f;
;     int* dumpi = (int*)(F.a->ws + WS_B + ((size_t)128 << 20));
.Lcvt_vcu:
	s_and_b32 s69, s41, 3
	s_lshl_b32 s41, s41, 3
	s_add_u32 s89, s41, s40
	s_lshl_b32 s71, s64, 3
	s_mul_i32 s39, s71, 12
	s_add_u32 s89, s89, s39
	s_movk_i32 s90, 8
	s_mov_b32 s32, 0
	s_add_u32 s86, s84, 0x9180000
	s_addc_u32 s87, s85, 0
	s_add_u32 s84, s84, 0x1100000
	s_addc_u32 s85, s85, 0
	s_add_u32 s14, s8, 0x900000
	s_addc_u32 s15, s9, 0
	s_add_u32 s16, s8, 0xb00000
	s_addc_u32 s17, s9, 0
	s_add_u32 s18, s8, 0xd00000
	s_addc_u32 s19, s9, 0
	v_mov_b32_e32 v131, 0
	s_add_u32 s20, s8, 0x4000
	v_mov_b32_e32 v133, v131
	s_addc_u32 s21, s9, 0
	v_lshl_add_u64 v[2:3], s[8:9], 0, v[132:133]
	s_mov_b64 s[8:9], 0x1d1c0000
	s_waitcnt vmcnt(0)
	v_lshl_add_u64 v[12:13], v[2:3], 0, s[8:9]
	s_mov_b64 s[8:9], 0x1d1c0100
	s_movk_i32 s4, 0x100
	v_mov_b32_e32 v135, v131
	v_lshl_add_u64 v[14:15], v[2:3], 0, s[8:9]
	s_mov_b64 s[8:9], 0x1d1c0200
	v_cmp_gt_i32_e64 s[4:5], s4, v1
	s_mov_b32 s26, 0
	v_lshl_add_u32 v22, v1, 2, 0
	s_lshl_b32 s27, s49, 5
	v_lshl_add_u64 v[10:11], s[6:7], 0, v[134:135]
	v_cmp_gt_u32_e64 s[6:7], 8, v130
	v_lshl_add_u64 v[16:17], v[2:3], 0, s[8:9]
	v_mov_b64_e32 v[18:19], 0x100
	v_mov_b64_e32 v[20:21], 0xff
	v_mov_b32_e32 v23, 0xff800000
	v_mov_b32_e32 v24, 1
	s_waitcnt vmcnt(0)
	s_barrier
	s_branch .LBB0_532

; __device__ __forceinline__ void router_topk(Frame& F, int tile) {
;     ...
;         const f32x4 lg = lgn;
;         {
;           const bool real = lane < 8 && i > 0; const size_t o = (size_t)(tok - 1) * 8 + lane;
;           int* de = real ? tk_e + o : dumpi + lane; float* dg = real ? tk_g + o : (float*)dumpi + 64 + lane; int* dp = real ? tk_p + o : dumpi + 128 + lane;
;           *de = pe; *dg = pg; *dp = pp; }
;         lgn = *(const f32x4*)(logits + (size_t)(i + 1 < 32 ? tok + 1 : tok) * 256 + 4 * lane);
.Lcvt_wd:
	v_mov_b64_e32 v[30:31], v[8:9]
	s_cmp_lg_u32 s24, 31
	v_mov_b64_e32 v[28:29], v[6:7]
	v_lshl_add_u64 v[6:7], s[30:31], 0, v[130:131]
	s_cselect_b64 s[30:31], -1, 0
	v_lshlrev_b64 v[6:7], 2, v[6:7]
	s_cmp_lg_u64 s[30:31], 0
	v_lshl_add_u64 v[8:9], s[14:15], 0, v[6:7]
	v_lshl_add_u64 v[32:33], s[16:17], 0, v[6:7]
	v_lshl_add_u64 v[6:7], s[18:19], 0, v[6:7]
	s_addc_u32 s8, s8, 0
	v_cndmask_b32_e32 v9, v13, v9, vcc
	v_cndmask_b32_e32 v8, v12, v8, vcc
	v_cndmask_b32_e32 v6, v16, v6, vcc
	s_ashr_i32 s9, s8, 31
	v_cndmask_b32_e32 v33, v15, v33, vcc
	v_cndmask_b32_e32 v32, v14, v32, vcc
	v_cndmask_b32_e32 v7, v17, v7, vcc
	global_store_dword v[8:9], v27, off
	global_store_dword v[32:33], v26, off
	s_waitcnt lgkmcnt(0)
	global_store_dword v[6:7], v25, off
	v_mul_f32_e32 v6, 0xbfb8aa3b, v28
	s_lshl_b64 s[8:9], s[8:9], 10
	v_exp_f32_e32 v28, v6
	v_lshl_add_u64 v[6:7], v[10:11], 0, s[8:9]
	global_load_dwordx4 v[6:9], v[6:7], off
	s_sub_u32 s69, s69, 1
	s_cmp_lt_i32 s69, 0
	s_cbranch_scc0 .Lcvt_none_l
	s_mov_b32 s69, 3
	s_cmp_eq_u32 s90, 0
	s_cbranch_scc1 .Lcvt_none_l
	s_cmp_lg_u32 s32, 0
	s_cbranch_scc1 .Lcvt_none_l
	s_sub_u32 s90, s90, 1
	s_lshr_b32 s39, s89, 6
	s_and_b32 s40, s89, 63
	s_mul_hi_u32 s42, s39, 0xaaaaaaab
	s_lshr_b32 s42, s42, 1
	s_mul_i32 s41, s42, 3
	s_sub_u32 s41, s39, s41
	s_cmp_lt_u32 s42, 256
	s_cselect_b32 s100, s42, 0
	s_cselect_b64 s[44:45], -1, 0
	s_lshl_b32 s100, s100, 20
	s_cmp_eq_u32 s41, 2
	s_cbranch_scc1 .Lcvt_down_l
	s_cmp_eq_u32 s41, 0
	s_cselect_b64 s[96:97], s[72:73], s[74:75]
	s_cselect_b64 s[98:99], s[78:79], s[80:81]
	s_mov_b32 s94, 0xc3317218
	s_cselect_b32 s94, 0xc2b8aa3b, s94
	s_cmp_lg_u64 s[44:45], 0
	s_cselect_b64 s[96:97], s[96:97], s[98:99]
	s_lshr_b32 s55, s40, 3
	s_and_b32 s58, s40, 7
	s_lshl_b32 s39, s55, 17
	s_add_u32 s100, s100, s39
	s_lshl_b32 s39, s58, 7
	s_add_u32 s100, s100, s39
	s_add_u32 s96, s96, s100
	s_addc_u32 s97, s97, 0
	s_lshl_b32 s42, s42, 19
	s_lshr_b32 s39, s58, 2
	s_lshl_b32 s39, s39, 18
	s_add_u32 s42, s42, s39
	s_and_b32 s39, s58, 3
	s_lshl_b32 s39, s39, 15
	s_add_u32 s42, s42, s39
	s_lshl_b32 s39, s41, 17
	s_add_u32 s42, s42, s39
	s_lshl_b32 s39, s55, 7
	s_add_u32 s42, s42, s39
	s_add_u32 s92, s84, s42
	s_addc_u32 s93, s85, 0
	s_movk_i32 s36, 0x400
	s_movk_i32 s38, 0x1000
	s_movk_i32 s98, 0x400
	s_branch .Lcvt_go_l
